# speedup vs baseline: 1.0079x; 1.0025x over previous
_Z12tailC_kernel5TailP:
	s_load_dwordx4 s[28:31], s[0:1], 0x198
	s_load_dwordx2 s[4:5], s[0:1], 0x188
	v_lshrrev_b32_e32 v1, 7, v0
	s_lshl_b32 s2, s2, 2
	v_bfe_u32 v3, v0, 4, 3
	v_or_b32_e32 v2, s2, v1
	v_lshl_or_b32 v6, s3, 3, v3
	v_ashrrev_i32_e32 v3, 31, v2
	s_movk_i32 s6, 0x1900
	s_waitcnt lgkmcnt(0)
	v_mov_b32_e32 v4, s28
	v_mov_b32_e32 v5, s29
	v_mad_i64_i32 v[6:7], s[6:7], v6, s6, v[2:3]
	s_movk_i32 s8, 0x48
	v_mad_u64_u32 v[4:5], s[6:7], v6, s8, v[4:5]
	v_mad_i32_i24 v5, v7, s8, v5
	s_movk_i32 s8, 0x3000
	v_add_co_u32_e32 v6, vcc, s8, v4
	s_movk_i32 s6, 0x7000
	s_nop 0
	v_addc_co_u32_e32 v7, vcc, 0, v5, vcc
	v_add_co_u32_e32 v8, vcc, s6, v4
	s_mov_b32 s6, 0xa000
	s_nop 0
	v_addc_co_u32_e32 v9, vcc, 0, v5, vcc
	v_add_co_u32_e32 v10, vcc, s6, v4
	s_mov_b32 s6, 0xe000
	s_nop 0
	v_addc_co_u32_e32 v11, vcc, 0, v5, vcc
	v_add_co_u32_e32 v12, vcc, s6, v4
	s_mov_b32 s6, 0x11000
	s_nop 0
	v_addc_co_u32_e32 v13, vcc, 0, v5, vcc
	v_add_co_u32_e32 v14, vcc, s6, v4
	s_mov_b32 s6, 0x15000
	s_nop 0
	v_addc_co_u32_e32 v15, vcc, 0, v5, vcc
	v_add_co_u32_e32 v16, vcc, s6, v4
	s_mov_b32 s6, 0x18000
	s_nop 0
	v_addc_co_u32_e32 v17, vcc, 0, v5, vcc
	v_add_co_u32_e32 v18, vcc, s6, v4
	s_mov_b32 s6, 0x1c000
	s_nop 0
	v_addc_co_u32_e32 v19, vcc, 0, v5, vcc
	v_add_co_u32_e32 v20, vcc, s6, v4
	s_mov_b32 s6, 0x1f000
	s_nop 0
	v_addc_co_u32_e32 v21, vcc, 0, v5, vcc
	v_add_co_u32_e32 v22, vcc, s6, v4
	s_mov_b32 s6, 0x23000
	s_nop 0
	v_addc_co_u32_e32 v23, vcc, 0, v5, vcc
	v_add_co_u32_e32 v24, vcc, s6, v4
	s_mov_b32 s6, 0x26000
	s_nop 0
	v_addc_co_u32_e32 v25, vcc, 0, v5, vcc
	v_add_co_u32_e32 v26, vcc, s6, v4
	s_mov_b32 s6, 0x2a000
	s_nop 0
	v_addc_co_u32_e32 v27, vcc, 0, v5, vcc
	v_add_co_u32_e32 v28, vcc, s6, v4
	s_mov_b32 s6, 0x2d000
	s_nop 0
	v_addc_co_u32_e32 v29, vcc, 0, v5, vcc
	global_load_dword v114, v[6:7], off offset:2176
	global_load_dwordx2 v[60:61], v[6:7], off offset:2112
	global_load_dword v114, v[8:9], off offset:192
	global_load_dwordx2 v[64:65], v[8:9], off offset:128
	global_load_dword v114, v[10:11], off offset:2304
	global_load_dwordx2 v[66:67], v[10:11], off offset:2240
	global_load_dword v114, v[12:13], off offset:320
	global_load_dwordx2 v[68:69], v[12:13], off offset:256
	s_nop 0
	global_load_dword v114, v[14:15], off offset:2432
	global_load_dwordx2 v[12:13], v[14:15], off offset:2368
	global_load_dword v114, v[16:17], off offset:448
	global_load_dwordx2 v[10:11], v[16:17], off offset:384
	global_load_dword v114, v[18:19], off offset:2560
	global_load_dwordx2 v[8:9], v[18:19], off offset:2496
	global_load_dword v114, v[20:21], off offset:576
	global_load_dwordx2 v[6:7], v[20:21], off offset:512
	s_nop 0
	global_load_dword v114, v[22:23], off offset:2688
	global_load_dwordx2 v[20:21], v[22:23], off offset:2624
	global_load_dword v114, v[24:25], off offset:704
	global_load_dwordx2 v[18:19], v[24:25], off offset:640
	global_load_dword v114, v[26:27], off offset:2816
	global_load_dwordx2 v[16:17], v[26:27], off offset:2752
	global_load_dword v114, v[28:29], off offset:832
	global_load_dwordx2 v[14:15], v[28:29], off offset:768
	v_add_co_u32_e32 v24, vcc, s6, v4
	s_mov_b32 s6, 0x31000
	s_nop 0
	v_addc_co_u32_e32 v25, vcc, 0, v5, vcc
	v_add_co_u32_e32 v32, vcc, s6, v4
	s_mov_b32 s6, 0x34000
	s_nop 0
	v_addc_co_u32_e32 v33, vcc, 0, v5, vcc
	v_add_co_u32_e32 v34, vcc, s6, v4
	s_mov_b32 s6, 0x38000
	s_nop 0
	v_addc_co_u32_e32 v35, vcc, 0, v5, vcc
	v_add_co_u32_e32 v36, vcc, s6, v4
	s_mov_b32 s6, 0x3b000
	s_nop 0
	v_addc_co_u32_e32 v37, vcc, 0, v5, vcc
	v_add_co_u32_e32 v38, vcc, s6, v4
	s_mov_b32 s6, 0x3f000
	s_nop 0
	v_addc_co_u32_e32 v39, vcc, 0, v5, vcc
	v_add_co_u32_e32 v40, vcc, s6, v4
	s_mov_b32 s6, 0x42000
	s_nop 0
	v_addc_co_u32_e32 v41, vcc, 0, v5, vcc
	v_add_co_u32_e32 v42, vcc, s6, v4
	s_mov_b32 s6, 0x46000
	s_nop 0
	v_addc_co_u32_e32 v43, vcc, 0, v5, vcc
	v_add_co_u32_e32 v44, vcc, s6, v4
	s_mov_b32 s6, 0x49000
	s_nop 0
	v_addc_co_u32_e32 v45, vcc, 0, v5, vcc
	v_add_co_u32_e32 v46, vcc, s6, v4
	s_mov_b32 s6, 0x4d000
	s_nop 0
	v_addc_co_u32_e32 v47, vcc, 0, v5, vcc
	v_add_co_u32_e32 v48, vcc, s6, v4
	s_mov_b32 s6, 0x50000
	s_nop 0
	v_addc_co_u32_e32 v49, vcc, 0, v5, vcc
	v_add_co_u32_e32 v50, vcc, s6, v4
	s_mov_b32 s6, 0x54000
	s_nop 0
	v_addc_co_u32_e32 v51, vcc, 0, v5, vcc
	v_add_co_u32_e32 v52, vcc, s6, v4
	s_mov_b32 s6, 0x57000
	s_nop 0
	v_addc_co_u32_e32 v53, vcc, 0, v5, vcc
	v_add_co_u32_e32 v54, vcc, s6, v4
	s_mov_b32 s6, 0x5b000
	s_nop 0
	v_addc_co_u32_e32 v55, vcc, 0, v5, vcc
	v_add_co_u32_e32 v56, vcc, s6, v4
	s_mov_b32 s6, 0x5e000
	s_nop 0
	v_addc_co_u32_e32 v57, vcc, 0, v5, vcc
	v_add_co_u32_e32 v58, vcc, s6, v4
	s_mov_b32 s6, 0x62000
	s_nop 0
	v_addc_co_u32_e32 v59, vcc, 0, v5, vcc
	v_add_co_u32_e32 v62, vcc, s6, v4
	global_load_dword v114, v[24:25], off offset:2944
	global_load_dwordx2 v[30:31], v[24:25], off offset:2880
	global_load_dword v114, v[32:33], off offset:960
	global_load_dwordx2 v[28:29], v[32:33], off offset:896
	global_load_dword v114, v[34:35], off offset:3072
	global_load_dwordx2 v[26:27], v[34:35], off offset:3008
	global_load_dword v114, v[36:37], off offset:1088
	global_load_dwordx2 v[22:23], v[36:37], off offset:1024
	s_nop 0
	global_load_dword v114, v[38:39], off offset:3200
	global_load_dwordx2 v[36:37], v[38:39], off offset:3136
	global_load_dword v114, v[40:41], off offset:1216
	global_load_dwordx2 v[34:35], v[40:41], off offset:1152
	global_load_dword v114, v[42:43], off offset:3328
	global_load_dwordx2 v[32:33], v[42:43], off offset:3264
	global_load_dword v114, v[44:45], off offset:1344
	global_load_dwordx2 v[24:25], v[44:45], off offset:1280
	s_nop 0
	global_load_dword v114, v[46:47], off offset:3456
	global_load_dwordx2 v[44:45], v[46:47], off offset:3392
	global_load_dword v114, v[48:49], off offset:1472
	global_load_dwordx2 v[42:43], v[48:49], off offset:1408
	global_load_dword v114, v[50:51], off offset:3584
	global_load_dwordx2 v[40:41], v[50:51], off offset:3520
	global_load_dword v114, v[52:53], off offset:1600
	global_load_dwordx2 v[38:39], v[52:53], off offset:1536
	v_addc_co_u32_e32 v63, vcc, 0, v5, vcc
	global_load_dword v114, v[54:55], off offset:3712
	global_load_dwordx2 v[52:53], v[54:55], off offset:3648
	global_load_dword v114, v[56:57], off offset:1728
	global_load_dwordx2 v[50:51], v[56:57], off offset:1664
	global_load_dword v114, v[58:59], off offset:3840
	global_load_dwordx2 v[48:49], v[58:59], off offset:3776
	global_load_dword v114, v[62:63], off offset:1856
	global_load_dwordx2 v[46:47], v[62:63], off offset:1792
	global_load_dword v114, v[4:5], off offset:64
	global_load_dwordx2 v[70:71], v[4:5], off
	s_mov_b32 s6, 0x65000
	v_add_co_u32_e32 v62, vcc, s6, v4
	s_mov_b32 s6, 0x69000
	s_nop 0
	v_addc_co_u32_e32 v63, vcc, 0, v5, vcc
	v_add_co_u32_e32 v72, vcc, s6, v4
	s_mov_b32 s6, 0x6c000
	s_nop 0
	v_addc_co_u32_e32 v73, vcc, 0, v5, vcc
	v_add_co_u32_e32 v74, vcc, s6, v4
	s_mov_b32 s6, 0xff800000
	s_nop 0
	v_addc_co_u32_e32 v75, vcc, 0, v5, vcc
	global_load_dword v114, v[62:63], off offset:3968
	global_load_dwordx2 v[58:59], v[62:63], off offset:3904
	global_load_dword v114, v[72:73], off offset:1984
	global_load_dwordx2 v[56:57], v[72:73], off offset:1920
	global_load_dwordx2 v[54:55], v[74:75], off offset:4032
	v_and_b32_e32 v62, 15, v0
	v_lshlrev_b32_e32 v62, 2, v62
	v_mov_b32_e32 v63, 0
	v_lshl_add_u64 v[72:73], v[4:5], 0, v[62:63]
	s_load_dwordx8 s[20:27], s[0:1], 0x130
	s_mul_i32 s28, s3, 0xc8
	v_add_u32_e32 v2, s28, v2
	s_waitcnt vmcnt(3)
	v_max3_f32 v3, v70, s6, v60
	v_max3_f32 v3, v3, v64, v66
	v_max3_f32 v3, v3, v68, v12
	v_max3_f32 v3, v3, v10, v8
	v_max3_f32 v3, v3, v6, v20
	v_max3_f32 v3, v3, v18, v16
	v_max3_f32 v3, v3, v14, v30
	v_max3_f32 v3, v3, v28, v26
	v_max3_f32 v3, v3, v22, v36
	v_max3_f32 v3, v3, v34, v32
	v_max3_f32 v3, v3, v24, v44
	v_max3_f32 v3, v3, v42, v40
	v_max3_f32 v3, v3, v38, v52
	v_max3_f32 v3, v3, v50, v48
	s_mov_b64 s[6:7], 0x3840
	s_waitcnt vmcnt(2)
	v_max3_f32 v3, v3, v46, v58
	s_waitcnt vmcnt(0)
	v_max3_f32 v3, v3, v56, v54
	v_sub_f32_e32 v80, v70, v3
	global_load_dword v70, v[72:73], off offset:8
	v_lshl_add_u64 v[72:73], v[4:5], 0, s[6:7]
	s_mov_b64 s[6:7], 0x7080
	v_lshl_add_u64 v[74:75], v[4:5], 0, s[6:7]
	s_mov_b64 s[6:7], 0xa8c0
	v_lshl_add_u64 v[76:77], v[4:5], 0, s[6:7]
	s_mov_b64 s[6:7], 0xe100
	v_lshl_add_u64 v[72:73], v[72:73], 0, v[62:63]
	v_lshl_add_u64 v[78:79], v[4:5], 0, s[6:7]
	v_sub_f32_e32 v81, v60, v3
	v_lshl_add_u64 v[74:75], v[74:75], 0, v[62:63]
	v_sub_f32_e32 v82, v64, v3
	v_lshl_add_u64 v[76:77], v[76:77], 0, v[62:63]
	v_sub_f32_e32 v83, v66, v3
	v_lshl_add_u64 v[78:79], v[78:79], 0, v[62:63]
	v_sub_f32_e32 v84, v68, v3
	global_load_dword v60, v[72:73], off offset:8
	global_load_dword v64, v[74:75], off offset:8
	global_load_dword v66, v[76:77], off offset:8
	global_load_dword v68, v[78:79], off offset:8
	s_mov_b64 s[6:7], 0x11940
	v_lshl_add_u64 v[72:73], v[4:5], 0, s[6:7]
	s_mov_b64 s[6:7], 0x15180
	v_lshl_add_u64 v[74:75], v[4:5], 0, s[6:7]
	s_mov_b64 s[6:7], 0x189c0
	v_lshl_add_u64 v[72:73], v[72:73], 0, v[62:63]
	v_lshl_add_u64 v[76:77], v[4:5], 0, s[6:7]
	v_exp_f32_e32 v78, v80
	v_sub_f32_e32 v85, v12, v3
	v_lshl_add_u64 v[74:75], v[74:75], 0, v[62:63]
	v_sub_f32_e32 v86, v10, v3
	v_lshl_add_u64 v[76:77], v[76:77], 0, v[62:63]
	v_sub_f32_e32 v87, v8, v3
	global_load_dword v12, v[72:73], off offset:8
	global_load_dword v10, v[74:75], off offset:8
	global_load_dword v8, v[76:77], off offset:8
	v_exp_f32_e32 v72, v81
	v_exp_f32_e32 v74, v82
	v_exp_f32_e32 v76, v83
	s_mov_b64 s[6:7], 0x1c200
	v_sub_f32_e32 v80, v6, v3
	v_sub_f32_e32 v81, v20, v3
	v_sub_f32_e32 v82, v18, v3
	v_sub_f32_e32 v83, v16, v3
	v_sub_f32_e32 v88, v30, v3
	v_sub_f32_e32 v89, v28, v3
	v_sub_f32_e32 v90, v26, v3
	v_sub_f32_e32 v91, v34, v3
	v_sub_f32_e32 v92, v32, v3
	v_sub_f32_e32 v93, v24, v3
	s_waitcnt vmcnt(7)
	v_pk_fma_f32 v[70:71], v[78:79], v[70:71], 0 op_sel_hi:[0,1,0]
	v_exp_f32_e32 v78, v84
	v_sub_f32_e32 v84, v14, v3
	s_waitcnt vmcnt(6)
	v_pk_fma_f32 v[60:61], v[72:73], v[60:61], v[70:71] op_sel_hi:[0,1,1]
	s_waitcnt vmcnt(5)
	v_pk_fma_f32 v[60:61], v[74:75], v[64:65], v[60:61] op_sel_hi:[0,1,1]
	v_lshl_add_u64 v[64:65], v[4:5], 0, s[6:7]
	s_mov_b64 s[6:7], 0x1fa40
	s_waitcnt vmcnt(4)
	v_pk_fma_f32 v[60:61], v[76:77], v[66:67], v[60:61] op_sel_hi:[0,1,1]
	v_lshl_add_u64 v[66:67], v[4:5], 0, s[6:7]
	s_mov_b64 s[6:7], 0x23280
	s_waitcnt vmcnt(3)
	v_pk_fma_f32 v[60:61], v[78:79], v[68:69], v[60:61] op_sel_hi:[0,1,1]
	v_lshl_add_u64 v[68:69], v[4:5], 0, s[6:7]
	s_mov_b64 s[6:7], 0x26ac0
	v_lshl_add_u64 v[70:71], v[4:5], 0, s[6:7]
	s_mov_b64 s[6:7], 0x2a300
	v_lshl_add_u64 v[72:73], v[4:5], 0, s[6:7]
	s_mov_b64 s[6:7], 0x2db40
	v_lshl_add_u64 v[74:75], v[4:5], 0, s[6:7]
	s_mov_b64 s[6:7], 0x31380
	v_lshl_add_u64 v[76:77], v[4:5], 0, s[6:7]
	s_mov_b64 s[6:7], 0x34bc0
	v_lshl_add_u64 v[64:65], v[64:65], 0, v[62:63]
	v_lshl_add_u64 v[78:79], v[4:5], 0, s[6:7]
	s_mov_b64 s[6:7], 0x38400
	v_lshl_add_u64 v[66:67], v[66:67], 0, v[62:63]
	v_lshl_add_u64 v[68:69], v[68:69], 0, v[62:63]
	v_lshl_add_u64 v[70:71], v[70:71], 0, v[62:63]
	v_lshl_add_u64 v[72:73], v[72:73], 0, v[62:63]
	v_lshl_add_u64 v[74:75], v[74:75], 0, v[62:63]
	v_lshl_add_u64 v[76:77], v[76:77], 0, v[62:63]
	v_lshl_add_u64 v[78:79], v[78:79], 0, v[62:63]
	global_load_dword v6, v[64:65], off offset:8
	global_load_dword v20, v[66:67], off offset:8
	global_load_dword v18, v[68:69], off offset:8
	global_load_dword v16, v[70:71], off offset:8
	global_load_dword v14, v[72:73], off offset:8
	global_load_dword v30, v[74:75], off offset:8
	global_load_dword v28, v[76:77], off offset:8
	global_load_dword v26, v[78:79], off offset:8
	v_lshl_add_u64 v[64:65], v[4:5], 0, s[6:7]
	s_mov_b64 s[6:7], 0x3bc40
	v_lshl_add_u64 v[66:67], v[4:5], 0, s[6:7]
	s_mov_b64 s[6:7], 0x3f480
	v_lshl_add_u64 v[68:69], v[4:5], 0, s[6:7]
	s_mov_b64 s[6:7], 0x42cc0
	v_lshl_add_u64 v[70:71], v[4:5], 0, s[6:7]
	s_mov_b64 s[6:7], 0x46500
	v_lshl_add_u64 v[72:73], v[4:5], 0, s[6:7]
	s_mov_b64 s[6:7], 0x49d40
	v_lshl_add_u64 v[64:65], v[64:65], 0, v[62:63]
	v_lshl_add_u64 v[74:75], v[4:5], 0, s[6:7]
	s_mov_b64 s[6:7], 0x4d580
	v_sub_f32_e32 v78, v22, v3
	v_sub_f32_e32 v79, v36, v3
	v_lshl_add_u64 v[66:67], v[66:67], 0, v[62:63]
	global_load_dword v22, v[64:65], off offset:8
	global_load_dword v36, v[66:67], off offset:8
	v_lshl_add_u64 v[76:77], v[4:5], 0, s[6:7]
	s_mov_b64 s[6:7], 0x50dc0
	v_lshl_add_u64 v[64:65], v[68:69], 0, v[62:63]
	v_lshl_add_u64 v[66:67], v[4:5], 0, s[6:7]
	s_mov_b64 s[6:7], 0x54600
	v_lshl_add_u64 v[68:69], v[70:71], 0, v[62:63]
	global_load_dword v34, v[64:65], off offset:8
	global_load_dword v32, v[68:69], off offset:8
	v_lshl_add_u64 v[64:65], v[72:73], 0, v[62:63]
	v_lshl_add_u64 v[68:69], v[4:5], 0, s[6:7]
	s_mov_b64 s[6:7], 0x57e40
	v_lshl_add_u64 v[70:71], v[74:75], 0, v[62:63]
	v_sub_f32_e32 v72, v44, v3
	global_load_dword v24, v[64:65], off offset:8
	global_load_dword v44, v[70:71], off offset:8
	v_lshl_add_u64 v[64:65], v[76:77], 0, v[62:63]
	v_lshl_add_u64 v[70:71], v[4:5], 0, s[6:7]
	s_mov_b64 s[6:7], 0x5b680
	v_lshl_add_u64 v[66:67], v[66:67], 0, v[62:63]
	v_sub_f32_e32 v73, v42, v3
	v_sub_f32_e32 v74, v40, v3
	global_load_dword v42, v[64:65], off offset:8
	global_load_dword v40, v[66:67], off offset:8
	v_lshl_add_u64 v[64:65], v[68:69], 0, v[62:63]
	v_lshl_add_u64 v[66:67], v[4:5], 0, s[6:7]
	s_mov_b64 s[6:7], 0x5eec0
	v_sub_f32_e32 v75, v38, v3
	v_sub_f32_e32 v76, v52, v3
	v_lshl_add_u64 v[68:69], v[70:71], 0, v[62:63]
	global_load_dword v38, v[64:65], off offset:8
	global_load_dword v52, v[68:69], off offset:8
	v_lshl_add_u64 v[64:65], v[66:67], 0, v[62:63]
	v_lshl_add_u64 v[66:67], v[4:5], 0, s[6:7]
	s_mov_b64 s[6:7], 0x62700
	v_sub_f32_e32 v68, v50, v3
	v_sub_f32_e32 v69, v48, v3
	v_lshl_add_u64 v[66:67], v[66:67], 0, v[62:63]
	global_load_dword v50, v[64:65], off offset:8
	global_load_dword v48, v[66:67], off offset:8
	v_lshl_add_u64 v[64:65], v[4:5], 0, s[6:7]
	v_lshl_add_u64 v[64:65], v[64:65], 0, v[62:63]
	s_mov_b64 s[6:7], 0x65f40
	v_sub_f32_e32 v66, v46, v3
	global_load_dword v46, v[64:65], off offset:8
	v_lshl_add_u64 v[64:65], v[4:5], 0, s[6:7]
	v_lshl_add_u64 v[64:65], v[64:65], 0, v[62:63]
	s_mov_b64 s[6:7], 0x69780
	v_sub_f32_e32 v67, v58, v3
	global_load_dword v58, v[64:65], off offset:8
	v_lshl_add_u64 v[64:65], v[4:5], 0, s[6:7]
	s_mov_b64 s[6:7], 0x6cfc0
	v_lshl_add_u64 v[64:65], v[64:65], 0, v[62:63]
	v_lshl_add_u64 v[4:5], v[4:5], 0, s[6:7]
	v_sub_f32_e32 v70, v56, v3
	global_load_dword v56, v[64:65], off offset:8
	v_lshl_add_u64 v[4:5], v[4:5], 0, v[62:63]
	v_sub_f32_e32 v3, v54, v3
	global_load_dword v54, v[4:5], off offset:8
	v_exp_f32_e32 v4, v85
	v_exp_f32_e32 v62, v86
	v_exp_f32_e32 v64, v87
	s_waitcnt vmcnt(26)
	v_pk_fma_f32 v[4:5], v[4:5], v[12:13], v[60:61] op_sel_hi:[0,1,1]
	s_waitcnt vmcnt(25)
	v_pk_fma_f32 v[4:5], v[62:63], v[10:11], v[4:5] op_sel_hi:[0,1,1]
	s_waitcnt vmcnt(24)
	v_pk_fma_f32 v[4:5], v[64:65], v[8:9], v[4:5] op_sel_hi:[0,1,1]
	v_exp_f32_e32 v8, v80
	v_exp_f32_e32 v10, v81
	v_exp_f32_e32 v12, v82
	v_exp_f32_e32 v60, v83
	s_waitcnt vmcnt(23)
	v_pk_fma_f32 v[4:5], v[8:9], v[6:7], v[4:5] op_sel_hi:[0,1,1]
	v_exp_f32_e32 v6, v84
	s_waitcnt vmcnt(22)
	v_pk_fma_f32 v[4:5], v[10:11], v[20:21], v[4:5] op_sel_hi:[0,1,1]
	v_exp_f32_e32 v8, v88
	s_waitcnt vmcnt(21)
	v_pk_fma_f32 v[4:5], v[12:13], v[18:19], v[4:5] op_sel_hi:[0,1,1]
	v_exp_f32_e32 v10, v89
	s_waitcnt vmcnt(20)
	v_pk_fma_f32 v[4:5], v[60:61], v[16:17], v[4:5] op_sel_hi:[0,1,1]
	v_exp_f32_e32 v12, v90
	s_waitcnt vmcnt(19)
	v_pk_fma_f32 v[4:5], v[6:7], v[14:15], v[4:5] op_sel_hi:[0,1,1]
	v_exp_f32_e32 v6, v78
	s_waitcnt vmcnt(18)
	v_pk_fma_f32 v[4:5], v[8:9], v[30:31], v[4:5] op_sel_hi:[0,1,1]
	v_exp_f32_e32 v8, v79
	s_waitcnt vmcnt(17)
	v_pk_fma_f32 v[4:5], v[10:11], v[28:29], v[4:5] op_sel_hi:[0,1,1]
	v_exp_f32_e32 v10, v91
	s_waitcnt vmcnt(16)
	v_pk_fma_f32 v[4:5], v[12:13], v[26:27], v[4:5] op_sel_hi:[0,1,1]
	v_exp_f32_e32 v12, v92
	s_waitcnt vmcnt(15)
	v_pk_fma_f32 v[4:5], v[6:7], v[22:23], v[4:5] op_sel_hi:[0,1,1]
	v_exp_f32_e32 v6, v93
	s_waitcnt vmcnt(14)
	v_pk_fma_f32 v[4:5], v[8:9], v[36:37], v[4:5] op_sel_hi:[0,1,1]
	v_exp_f32_e32 v8, v72
	v_exp_f32_e32 v14, v75
	s_waitcnt vmcnt(13)
	v_pk_fma_f32 v[4:5], v[10:11], v[34:35], v[4:5] op_sel_hi:[0,1,1]
	v_exp_f32_e32 v10, v73
	s_waitcnt vmcnt(12)
	v_pk_fma_f32 v[4:5], v[12:13], v[32:33], v[4:5] op_sel_hi:[0,1,1]
	v_exp_f32_e32 v12, v74
	v_exp_f32_e32 v16, v76
	v_exp_f32_e32 v18, v68
	s_waitcnt vmcnt(11)
	v_pk_fma_f32 v[4:5], v[6:7], v[24:25], v[4:5] op_sel_hi:[0,1,1]
	s_waitcnt vmcnt(10)
	v_pk_fma_f32 v[4:5], v[8:9], v[44:45], v[4:5] op_sel_hi:[0,1,1]
	v_exp_f32_e32 v20, v69
	v_exp_f32_e32 v22, v66
	v_exp_f32_e32 v26, v67
	v_exp_f32_e32 v28, v70
	v_exp_f32_e32 v30, v3
	s_waitcnt vmcnt(9)
	v_pk_fma_f32 v[4:5], v[10:11], v[42:43], v[4:5] op_sel_hi:[0,1,1]
	s_waitcnt vmcnt(8)
	v_pk_fma_f32 v[4:5], v[12:13], v[40:41], v[4:5] op_sel_hi:[0,1,1]
	v_and_b32_e32 v70, 0x7f, v0
	v_lshlrev_b32_e32 v74, 10, v1
	s_waitcnt vmcnt(7)
	v_pk_fma_f32 v[4:5], v[14:15], v[38:39], v[4:5] op_sel_hi:[0,1,1]
	s_waitcnt vmcnt(6)
	v_pk_fma_f32 v[4:5], v[16:17], v[52:53], v[4:5] op_sel_hi:[0,1,1]
	s_waitcnt vmcnt(5)
	v_pk_fma_f32 v[4:5], v[18:19], v[50:51], v[4:5] op_sel_hi:[0,1,1]
	s_waitcnt vmcnt(4)
	v_pk_fma_f32 v[4:5], v[20:21], v[48:49], v[4:5] op_sel_hi:[0,1,1]
	s_waitcnt vmcnt(3)
	v_pk_fma_f32 v[4:5], v[22:23], v[46:47], v[4:5] op_sel_hi:[0,1,1]
	s_waitcnt vmcnt(2)
	v_pk_fma_f32 v[4:5], v[26:27], v[58:59], v[4:5] op_sel_hi:[0,1,1]
	s_waitcnt vmcnt(1)
	v_pk_fma_f32 v[4:5], v[28:29], v[56:57], v[4:5] op_sel_hi:[0,1,1]
	s_waitcnt vmcnt(0)
	v_pk_fma_f32 v[4:5], v[30:31], v[54:55], v[4:5] op_sel_hi:[0,1,1]
	v_div_scale_f32 v3, s[6:7], v5, v5, v4
	v_rcp_f32_e32 v6, v3
	s_movk_i32 s6, 0x2000
	v_fma_f32 v7, -v3, v6, 1.0
	v_fmac_f32_e32 v6, v7, v6
	v_div_scale_f32 v7, vcc, v4, v5, v4
	v_mul_f32_e32 v8, v7, v6
	v_fma_f32 v9, -v3, v8, v7
	v_fmac_f32_e32 v8, v9, v6
	v_fma_f32 v3, -v3, v8, v7
	v_div_fmas_f32 v3, v3, v6, v8
	v_div_fixup_f32 v3, v3, v5, v4
	v_lshlrev_b32_e32 v4, 2, v1
	v_lshl_or_b32 v4, v70, 4, v4
	ds_write_b32 v4, v3 offset:34816
	v_or_b32_e32 v3, v74, v70
	v_lshlrev_b32_e32 v62, 4, v3
	s_waitcnt lgkmcnt(0)
	s_barrier
	global_load_dwordx4 v[6:9], v62, s[20:21]
	global_load_dwordx4 v[10:13], v62, s[20:21] offset:2048
	v_lshl_add_u64 v[30:31], s[20:21], 0, v[62:63]
	v_add_co_u32_e32 v26, vcc, s6, v30
	s_movk_i32 s6, 0x1000
	s_nop 0
	v_addc_co_u32_e32 v27, vcc, 0, v31, vcc
	global_load_dwordx4 v[14:17], v[26:27], off offset:-4096
	v_add_co_u32_e32 v28, vcc, s6, v30
	v_lshlrev_b32_e32 v5, 9, v1
	s_nop 0
	v_addc_co_u32_e32 v29, vcc, 0, v31, vcc
	global_load_dwordx4 v[18:21], v[28:29], off offset:2048
	global_load_dwordx4 v[22:25], v[26:27], off
	v_add_co_u32_e32 v46, vcc, s8, v30
	global_load_dwordx4 v[26:29], v[26:27], off offset:2048
	s_nop 0
	v_addc_co_u32_e32 v47, vcc, 0, v31, vcc
	global_load_dwordx4 v[30:33], v[46:47], off
	ds_read_b128 v[34:37], v5 offset:34816
	ds_read_b128 v[38:41], v5 offset:34832
	ds_read_b128 v[42:45], v5 offset:34848
	global_load_dwordx4 v[46:49], v[46:47], off offset:2048
	ds_read_b128 v[50:53], v5 offset:34864
	s_load_dwordx2 s[6:7], s[0:1], 0x50
	v_ashrrev_i32_e32 v3, 31, v2
	v_lshlrev_b32_e32 v62, 2, v70
	v_lshlrev_b64 v[2:3], 9, v[2:3]
	v_lshl_or_b32 v71, v1, 11, v62
	s_movk_i32 s8, 0xfa00
	v_lshl_add_u64 v[2:3], s[4:5], 0, v[2:3]
	v_mad_i32_i24 v72, v1, s8, v71
	v_lshl_add_u64 v[2:3], v[2:3], 0, v[62:63]
	s_waitcnt vmcnt(7) lgkmcnt(0)
	v_pk_fma_f32 v[36:37], v[6:7], v[36:37], 0 op_sel_hi:[0,1,0]
	v_pk_fma_f32 v[36:37], v[6:7], v[40:41], v[36:37] op_sel:[1,0,0]
	v_pk_fma_f32 v[34:35], v[6:7], v[34:35], 0 op_sel_hi:[0,1,0]
	v_pk_fma_f32 v[44:45], v[8:9], v[44:45], v[36:37] op_sel_hi:[0,1,1]
	v_pk_fma_f32 v[6:7], v[6:7], v[38:39], v[34:35] op_sel:[1,0,0]
	ds_read_b128 v[34:37], v5 offset:34880
	ds_read_b128 v[38:41], v5 offset:34896
	v_pk_fma_f32 v[6:7], v[8:9], v[42:43], v[6:7] op_sel_hi:[0,1,1]
	v_mov_b32_e32 v8, v9
	v_pk_fma_f32 v[52:53], v[8:9], v[52:53], v[44:45] op_sel_hi:[0,1,1]
	v_pk_fma_f32 v[50:51], v[8:9], v[50:51], v[6:7] op_sel_hi:[0,1,1]
	ds_read_b128 v[6:9], v5 offset:34912
	ds_read_b128 v[42:45], v5 offset:34928
	s_waitcnt vmcnt(6) lgkmcnt(3)
	v_pk_fma_f32 v[36:37], v[10:11], v[36:37], v[52:53] op_sel_hi:[0,1,1]
	v_pk_fma_f32 v[34:35], v[10:11], v[34:35], v[50:51] op_sel_hi:[0,1,1]
	s_waitcnt lgkmcnt(2)
	v_pk_fma_f32 v[52:53], v[10:11], v[40:41], v[36:37] op_sel:[1,0,0]
	v_pk_fma_f32 v[10:11], v[10:11], v[38:39], v[34:35] op_sel:[1,0,0]
	ds_read_b128 v[34:37], v5 offset:34944
	ds_read_b128 v[38:41], v5 offset:34960
	v_mov_b32_e32 v50, v13
	s_waitcnt lgkmcnt(3)
	v_pk_fma_f32 v[52:53], v[12:13], v[8:9], v[52:53] op_sel_hi:[0,1,1]
	v_pk_fma_f32 v[54:55], v[12:13], v[6:7], v[10:11] op_sel_hi:[0,1,1]
	ds_read_b128 v[6:9], v5 offset:34976
	ds_read_b128 v[10:13], v5 offset:34992
	s_waitcnt lgkmcnt(4)
	v_pk_fma_f32 v[44:45], v[50:51], v[44:45], v[52:53] op_sel_hi:[0,1,1]
	s_waitcnt vmcnt(5) lgkmcnt(3)
	v_pk_fma_f32 v[52:53], v[14:15], v[36:37], v[44:45] op_sel_hi:[0,1,1]
	v_pk_fma_f32 v[36:37], v[50:51], v[42:43], v[54:55] op_sel_hi:[0,1,1]
	v_pk_fma_f32 v[50:51], v[14:15], v[34:35], v[36:37] op_sel_hi:[0,1,1]
	ds_read_b128 v[34:37], v5 offset:35008
	ds_read_b128 v[42:45], v5 offset:35024
	s_waitcnt lgkmcnt(4)
	v_pk_fma_f32 v[40:41], v[14:15], v[40:41], v[52:53] op_sel:[1,0,0]
	s_waitcnt lgkmcnt(3)
	v_pk_fma_f32 v[52:53], v[16:17], v[8:9], v[40:41] op_sel_hi:[0,1,1]
	v_pk_fma_f32 v[8:9], v[14:15], v[38:39], v[50:51] op_sel:[1,0,0]
	s_nop 0
	v_pk_fma_f32 v[14:15], v[16:17], v[6:7], v[8:9] op_sel_hi:[0,1,1]
	ds_read_b128 v[6:9], v5 offset:35040
	ds_read_b128 v[38:41], v5 offset:35056
	v_mov_b32_e32 v16, v17
	s_waitcnt lgkmcnt(4)
	v_pk_fma_f32 v[50:51], v[16:17], v[12:13], v[52:53] op_sel_hi:[0,1,1]
	v_pk_fma_f32 v[52:53], v[16:17], v[10:11], v[14:15] op_sel_hi:[0,1,1]
	ds_read_b128 v[10:13], v5 offset:35072
	ds_read_b128 v[14:17], v5 offset:35088
	s_waitcnt vmcnt(4) lgkmcnt(5)
	v_pk_fma_f32 v[36:37], v[18:19], v[36:37], v[50:51] op_sel_hi:[0,1,1]
	s_waitcnt lgkmcnt(4)
	v_pk_fma_f32 v[50:51], v[18:19], v[44:45], v[36:37] op_sel:[1,0,0]
	v_pk_fma_f32 v[34:35], v[18:19], v[34:35], v[52:53] op_sel_hi:[0,1,1]
	v_pk_fma_f32 v[18:19], v[18:19], v[42:43], v[34:35] op_sel:[1,0,0]
	v_mov_b32_e32 v52, v21
	s_waitcnt lgkmcnt(3)
	v_pk_fma_f32 v[50:51], v[20:21], v[8:9], v[50:51] op_sel_hi:[0,1,1]
	ds_read_b128 v[34:37], v5 offset:35104
	ds_read_b128 v[42:45], v5 offset:35120
	v_pk_fma_f32 v[54:55], v[20:21], v[6:7], v[18:19] op_sel_hi:[0,1,1]
	s_waitcnt lgkmcnt(4)
	v_pk_fma_f32 v[40:41], v[52:53], v[40:41], v[50:51] op_sel_hi:[0,1,1]
	s_waitcnt vmcnt(3) lgkmcnt(3)
	v_pk_fma_f32 v[50:51], v[22:23], v[12:13], v[40:41] op_sel_hi:[0,1,1]
	v_pk_fma_f32 v[12:13], v[52:53], v[38:39], v[54:55] op_sel_hi:[0,1,1]
	ds_read_b128 v[6:9], v5 offset:35136
	ds_read_b128 v[18:21], v5 offset:35152
	v_pk_fma_f32 v[52:53], v[22:23], v[10:11], v[12:13] op_sel_hi:[0,1,1]
	s_waitcnt lgkmcnt(4)
	v_pk_fma_f32 v[16:17], v[22:23], v[16:17], v[50:51] op_sel:[1,0,0]
	v_pk_fma_f32 v[14:15], v[22:23], v[14:15], v[52:53] op_sel:[1,0,0]
	ds_read_b128 v[10:13], v5 offset:35168
	ds_read_b128 v[38:41], v5 offset:35184
	s_waitcnt lgkmcnt(5)
	v_pk_fma_f32 v[50:51], v[24:25], v[36:37], v[16:17] op_sel_hi:[0,1,1]
	v_pk_fma_f32 v[22:23], v[24:25], v[34:35], v[14:15] op_sel_hi:[0,1,1]
	v_mov_b32_e32 v24, v25
	s_waitcnt lgkmcnt(4)
	v_pk_fma_f32 v[50:51], v[24:25], v[44:45], v[50:51] op_sel_hi:[0,1,1]
	ds_read_b128 v[14:17], v5 offset:35200
	ds_read_b128 v[34:37], v5 offset:35216
	s_waitcnt vmcnt(2) lgkmcnt(5)
	v_pk_fma_f32 v[8:9], v[26:27], v[8:9], v[50:51] op_sel_hi:[0,1,1]
	v_pk_fma_f32 v[52:53], v[24:25], v[42:43], v[22:23] op_sel_hi:[0,1,1]
	s_waitcnt lgkmcnt(4)
	v_pk_fma_f32 v[50:51], v[26:27], v[20:21], v[8:9] op_sel:[1,0,0]
	ds_read_b128 v[22:25], v5 offset:35232
	ds_read_b128 v[42:45], v5 offset:35248
	v_pk_fma_f32 v[6:7], v[26:27], v[6:7], v[52:53] op_sel_hi:[0,1,1]
	v_mov_b32_e32 v52, v29
	s_waitcnt lgkmcnt(5)
	v_pk_fma_f32 v[50:51], v[28:29], v[12:13], v[50:51] op_sel_hi:[0,1,1]
	s_waitcnt lgkmcnt(4)
	v_pk_fma_f32 v[40:41], v[52:53], v[40:41], v[50:51] op_sel_hi:[0,1,1]
	v_pk_fma_f32 v[26:27], v[26:27], v[18:19], v[6:7] op_sel:[1,0,0]
	ds_read_b128 v[6:9], v5 offset:35264
	ds_read_b128 v[18:21], v5 offset:35280
	s_waitcnt vmcnt(1) lgkmcnt(5)
	v_pk_fma_f32 v[16:17], v[30:31], v[16:17], v[40:41] op_sel_hi:[0,1,1]
	s_waitcnt lgkmcnt(4)
	v_pk_fma_f32 v[16:17], v[30:31], v[36:37], v[16:17] op_sel:[1,0,0]
	v_pk_fma_f32 v[54:55], v[28:29], v[10:11], v[26:27] op_sel_hi:[0,1,1]
	ds_read_b128 v[10:13], v5 offset:35296
	ds_read_b128 v[26:29], v5 offset:35312
	v_mov_b32_e32 v50, v33
	s_waitcnt lgkmcnt(5)
	v_pk_fma_f32 v[16:17], v[32:33], v[24:25], v[16:17] op_sel_hi:[0,1,1]
	s_waitcnt lgkmcnt(4)
	v_pk_fma_f32 v[16:17], v[50:51], v[44:45], v[16:17] op_sel_hi:[0,1,1]
	s_waitcnt vmcnt(0) lgkmcnt(3)
	v_pk_fma_f32 v[8:9], v[46:47], v[8:9], v[16:17] op_sel_hi:[0,1,1]
	v_pk_fma_f32 v[38:39], v[52:53], v[38:39], v[54:55] op_sel_hi:[0,1,1]
	s_waitcnt lgkmcnt(2)
	v_pk_fma_f32 v[8:9], v[46:47], v[20:21], v[8:9] op_sel:[1,0,0]
	s_waitcnt lgkmcnt(1)
	v_pk_fma_f32 v[8:9], v[48:49], v[12:13], v[8:9] op_sel_hi:[0,1,1]
	v_pk_fma_f32 v[12:13], v[30:31], v[14:15], v[38:39] op_sel_hi:[0,1,1]
	v_pk_fma_f32 v[12:13], v[30:31], v[34:35], v[12:13] op_sel:[1,0,0]
	s_nop 0
	v_pk_fma_f32 v[12:13], v[32:33], v[22:23], v[12:13] op_sel_hi:[0,1,1]
	v_pk_fma_f32 v[12:13], v[50:51], v[42:43], v[12:13] op_sel_hi:[0,1,1]
	v_pk_fma_f32 v[6:7], v[46:47], v[6:7], v[12:13] op_sel_hi:[0,1,1]
	v_pk_fma_f32 v[6:7], v[46:47], v[18:19], v[6:7] op_sel:[1,0,0]
	s_nop 0
	v_pk_fma_f32 v[6:7], v[48:49], v[10:11], v[6:7] op_sel_hi:[0,1,1]
	v_mov_b32_e32 v10, v49
	s_waitcnt lgkmcnt(0)
	v_pk_fma_f32 v[6:7], v[10:11], v[26:27], v[6:7] op_sel_hi:[0,1,1]
	v_pk_fma_f32 v[8:9], v[10:11], v[28:29], v[8:9] op_sel_hi:[0,1,1]
	ds_write2st64_b32 v71, v6, v7 offset1:2
	ds_write2st64_b32 v71, v8, v9 offset0:4 offset1:6
	s_waitcnt lgkmcnt(0)
	s_barrier
	ds_read2st64_b32 v[6:7], v72 offset1:8
	ds_read2st64_b32 v[8:9], v72 offset0:16 offset1:24
	s_waitcnt lgkmcnt(0)
	s_barrier
	global_load_dword v10, v[2:3], off
	global_load_dword v11, v62, s[6:7]
	s_load_dwordx16 s[4:19], s[0:1], 0x68
	s_waitcnt lgkmcnt(0)
	global_load_dword v2, v62, s[4:5]
	global_load_dword v84, v62, s[6:7]
	v_add_f32_e32 v3, v6, v7
	v_mbcnt_lo_u32_b32 v6, -1, 0
	v_mbcnt_hi_u32_b32 v6, -1, v6
	v_and_b32_e32 v7, 64, v6
	v_add_f32_e32 v3, v3, v8
	v_add_u32_e32 v8, 64, v7
	v_xor_b32_e32 v7, 32, v6
	v_add_f32_e32 v3, v3, v9
	v_cmp_lt_i32_e32 vcc, v7, v8
	v_xor_b32_e32 v9, 16, v6
	s_waitcnt vmcnt(3)
	v_add_f32_e32 v3, v3, v10
	v_cndmask_b32_e32 v7, v6, v7, vcc
	s_waitcnt vmcnt(2)
	v_add_f32_e32 v3, v3, v11
	v_lshlrev_b32_e32 v75, 2, v7
	ds_bpermute_b32 v7, v75, v3
	v_cmp_lt_i32_e32 vcc, v9, v8
	s_waitcnt lgkmcnt(0)
	v_add_f32_e32 v7, v3, v7
	v_cndmask_b32_e32 v9, v6, v9, vcc
	v_lshlrev_b32_e32 v76, 2, v9
	ds_bpermute_b32 v9, v76, v7
	s_waitcnt lgkmcnt(0)
	v_add_f32_e32 v7, v7, v9
	v_xor_b32_e32 v9, 8, v6
	v_cmp_lt_i32_e32 vcc, v9, v8
	s_nop 1
	v_cndmask_b32_e32 v9, v6, v9, vcc
	v_lshlrev_b32_e32 v77, 2, v9
	ds_bpermute_b32 v9, v77, v7
	s_waitcnt lgkmcnt(0)
	v_add_f32_e32 v7, v7, v9
	v_xor_b32_e32 v9, 4, v6
	v_cmp_lt_i32_e32 vcc, v9, v8
	s_nop 1
	v_cndmask_b32_e32 v9, v6, v9, vcc
	v_lshlrev_b32_e32 v78, 2, v9
	ds_bpermute_b32 v9, v78, v7
	s_waitcnt lgkmcnt(0)
	v_add_f32_e32 v7, v7, v9
	v_xor_b32_e32 v9, 2, v6
	v_cmp_lt_i32_e32 vcc, v9, v8
	s_nop 1
	v_cndmask_b32_e32 v9, v6, v9, vcc
	v_lshlrev_b32_e32 v81, 2, v9
	ds_bpermute_b32 v9, v81, v7
	s_waitcnt lgkmcnt(0)
	v_add_f32_e32 v7, v7, v9
	v_xor_b32_e32 v9, 1, v6
	v_cmp_lt_i32_e32 vcc, v9, v8
	s_nop 1
	v_cndmask_b32_e32 v6, v6, v9, vcc
	v_lshlrev_b32_e32 v83, 2, v6
	ds_bpermute_b32 v8, v83, v7
	v_lshrrev_b32_e32 v6, 6, v0
	v_and_b32_e32 v9, 63, v0
	v_cmp_eq_u32_e32 vcc, 0, v9
	v_lshlrev_b32_e32 v79, 2, v6
	s_and_saveexec_b64 s[4:5], vcc
	s_cbranch_execz .LBB13_2
	s_waitcnt lgkmcnt(0)
	v_add_f32_e32 v7, v7, v8
	ds_write_b32 v79, v7 offset:36864

	.amdhsa_kernel _Z12tailC_kernel5TailP
		.amdhsa_group_segment_fixed_size 36896
		.amdhsa_private_segment_fixed_size 0
		.amdhsa_kernarg_size 424
		.amdhsa_user_sgpr_count 2
		.amdhsa_user_sgpr_dispatch_ptr 0
		.amdhsa_user_sgpr_queue_ptr 0
		.amdhsa_user_sgpr_kernarg_segment_ptr 1
		.amdhsa_user_sgpr_dispatch_id 0
		.amdhsa_user_sgpr_kernarg_preload_length 0
		.amdhsa_user_sgpr_kernarg_preload_offset 0
		.amdhsa_user_sgpr_private_segment_size 0
		.amdhsa_uses_dynamic_stack 0
		.amdhsa_enable_private_segment 0
		.amdhsa_system_sgpr_workgroup_id_x 1
		.amdhsa_system_sgpr_workgroup_id_y 1
		.amdhsa_system_sgpr_workgroup_id_z 0
		.amdhsa_system_sgpr_workgroup_info 0
		.amdhsa_system_vgpr_workitem_id 0
		.amdhsa_next_free_vgpr 115
		.amdhsa_next_free_sgpr 52
		.amdhsa_accum_offset 116
		.amdhsa_reserve_vcc 1
		.amdhsa_float_round_mode_32 0
		.amdhsa_float_round_mode_16_64 0
		.amdhsa_float_denorm_mode_32 3
		.amdhsa_float_denorm_mode_16_64 3
		.amdhsa_dx10_clamp 1
		.amdhsa_ieee_mode 1
		.amdhsa_fp16_overflow 0
		.amdhsa_tg_split 0
		.amdhsa_exception_fp_ieee_invalid_op 0
		.amdhsa_exception_fp_denorm_src 0
		.amdhsa_exception_fp_ieee_div_zero 0
		.amdhsa_exception_fp_ieee_overflow 0
		.amdhsa_exception_fp_ieee_underflow 0
		.amdhsa_exception_fp_ieee_inexact 0
		.amdhsa_exception_int_div_zero 0
	.end_amdhsa_kernel

amdhsa.kernels:
  - .agpr_count:     0
    .args:
      - .actual_access:  read_only
        .address_space:  global
        .offset:         0
        .size:           8
        .value_kind:     global_buffer
      - .actual_access:  write_only
        .address_space:  global
        .offset:         8
        .size:           8
        .value_kind:     global_buffer
    .group_segment_fixed_size: 0
    .kernarg_segment_align: 8
    .kernarg_segment_size: 16
    .language:       OpenCL C
    .language_version:
      - 2
      - 0
    .max_flat_workgroup_size: 256
    .name:           _Z13prep_x_kernelPKfP15HIP_vector_typeIjLj4EE
    .private_segment_fixed_size: 0
    .sgpr_count:     23
    .sgpr_spill_count: 0
    .symbol:         _Z13prep_x_kernelPKfP15HIP_vector_typeIjLj4EE.kd
    .uniform_work_group_size: 1
    .uses_dynamic_stack: false
    .vgpr_count:     36
    .vgpr_spill_count: 0
    .wavefront_size: 64
  - .agpr_count:     0
    .args:
      - .actual_access:  read_only
        .address_space:  global
        .offset:         0
        .size:           8
        .value_kind:     global_buffer
      - .actual_access:  write_only
        .address_space:  global
        .offset:         8
        .size:           8
        .value_kind:     global_buffer
      - .offset:         16
        .size:           4
        .value_kind:     by_value
      - .offset:         20
        .size:           4
        .value_kind:     by_value
      - .offset:         24
        .size:           4
        .value_kind:     by_value
      - .offset:         28
        .size:           4
        .value_kind:     by_value
    .group_segment_fixed_size: 0
    .kernarg_segment_align: 8
    .kernarg_segment_size: 32
    .language:       OpenCL C
    .language_version:
      - 2
      - 0
    .max_flat_workgroup_size: 256
    .name:           _Z13prep_w_kernelPKfP15HIP_vector_typeIjLj4EEiiii
    .private_segment_fixed_size: 0
    .sgpr_count:     15
    .sgpr_spill_count: 0
    .symbol:         _Z13prep_w_kernelPKfP15HIP_vector_typeIjLj4EEiiii.kd
    .uniform_work_group_size: 1
    .uses_dynamic_stack: false
    .vgpr_count:     34
    .vgpr_spill_count: 0
    .wavefront_size: 64
  - .agpr_count:     0
    .args:
      - .actual_access:  write_only
        .address_space:  global
        .offset:         0
        .size:           8
        .value_kind:     global_buffer
    .group_segment_fixed_size: 0
    .kernarg_segment_align: 8
    .kernarg_segment_size: 8
    .language:       OpenCL C
    .language_version:
      - 2
      - 0
    .max_flat_workgroup_size: 256
    .name:           _Z18zero_border_kernelP15HIP_vector_typeIjLj4EE
    .private_segment_fixed_size: 0
    .sgpr_count:     12
    .sgpr_spill_count: 0
    .symbol:         _Z18zero_border_kernelP15HIP_vector_typeIjLj4EE.kd
    .uniform_work_group_size: 1
    .uses_dynamic_stack: false
    .vgpr_count:     6
    .vgpr_spill_count: 0
    .wavefront_size: 64
  - .agpr_count:     0
    .args:
      - .actual_access:  read_only
        .address_space:  global
        .offset:         0
        .size:           8
        .value_kind:     global_buffer
      - .address_space:  global
        .offset:         8
        .size:           8
        .value_kind:     global_buffer
      - .actual_access:  read_only
        .address_space:  global
        .offset:         16
        .size:           8
        .value_kind:     global_buffer
      - .actual_access:  read_only
        .address_space:  global
        .offset:         24
        .size:           8
        .value_kind:     global_buffer
      - .actual_access:  read_only
        .address_space:  global
        .offset:         32
        .size:           8
        .value_kind:     global_buffer
      - .actual_access:  write_only
        .address_space:  global
        .offset:         40
        .size:           8
        .value_kind:     global_buffer
    .group_segment_fixed_size: 154880
    .kernarg_segment_align: 8
    .kernarg_segment_size: 48
    .language:       OpenCL C
    .language_version:
      - 2
      - 0
    .max_flat_workgroup_size: 512
    .name:           _Z12conv1_kernelPKfPK15HIP_vector_typeIjLj4EES0_S0_S0_PDF16_
    .private_segment_fixed_size: 0
    .sgpr_count:     46
    .sgpr_spill_count: 0
    .symbol:         _Z12conv1_kernelPKfPK15HIP_vector_typeIjLj4EES0_S0_S0_PDF16_.kd
    .uniform_work_group_size: 1
    .uses_dynamic_stack: false
    .vgpr_count:     256
    .vgpr_spill_count: 0
    .wavefront_size: 64
  - .agpr_count:     0
    .args:
      - .actual_access:  read_only
        .address_space:  global
        .offset:         0
        .size:           8
        .value_kind:     global_buffer
      - .actual_access:  read_only
        .address_space:  global
        .offset:         8
        .size:           8
        .value_kind:     global_buffer
      - .actual_access:  read_only
        .address_space:  global
        .offset:         16
        .size:           8
        .value_kind:     global_buffer
      - .actual_access:  write_only
        .address_space:  global
        .offset:         24
        .size:           8
        .value_kind:     global_buffer
      - .actual_access:  write_only
        .address_space:  global
        .offset:         32
        .size:           8
        .value_kind:     global_buffer
    .group_segment_fixed_size: 116480
    .kernarg_segment_align: 8
    .kernarg_segment_size: 40
    .language:       OpenCL C
    .language_version:
      - 2
      - 0
    .max_flat_workgroup_size: 512
    .name:           _Z12conv3_kernelPK15HIP_vector_typeIjLj4EES2_PKfPfS5_
    .private_segment_fixed_size: 0
    .sgpr_count:     22
    .sgpr_spill_count: 0
    .symbol:         _Z12conv3_kernelPK15HIP_vector_typeIjLj4EES2_PKfPfS5_.kd
    .uniform_work_group_size: 1
    .uses_dynamic_stack: false
    .vgpr_count:     122
    .vgpr_spill_count: 0
    .wavefront_size: 64
  - .agpr_count:     0
    .args:
      - .actual_access:  read_only
        .address_space:  global
        .offset:         0
        .size:           8
        .value_kind:     global_buffer
      - .actual_access:  read_only
        .address_space:  global
        .offset:         8
        .size:           8
        .value_kind:     global_buffer
      - .actual_access:  write_only
        .address_space:  global
        .offset:         16
        .size:           8
        .value_kind:     global_buffer
      - .address_space:  global
        .offset:         24
        .size:           8
        .value_kind:     global_buffer
    .group_segment_fixed_size: 32768
    .kernarg_segment_align: 8
    .kernarg_segment_size: 32
    .language:       OpenCL C
    .language_version:
      - 2
      - 0
    .max_flat_workgroup_size: 256
    .name:           _Z15nms_hist_kernelPKfS0_PjS1_
    .private_segment_fixed_size: 0
    .sgpr_count:     102
    .sgpr_spill_count: 0
    .symbol:         _Z15nms_hist_kernelPKfS0_PjS1_.kd
    .uniform_work_group_size: 1
    .uses_dynamic_stack: false
    .vgpr_count:     128
    .vgpr_spill_count: 0
    .wavefront_size: 64
  - .agpr_count:     0
    .args:
      - .actual_access:  read_only
        .address_space:  global
        .offset:         0
        .size:           8
        .value_kind:     global_buffer
      - .actual_access:  write_only
        .address_space:  global
        .offset:         8
        .size:           8
        .value_kind:     global_buffer
    .group_segment_fixed_size: 4096
    .kernarg_segment_align: 8
    .kernarg_segment_size: 16
    .language:       OpenCL C
    .language_version:
      - 2
      - 0
    .max_flat_workgroup_size: 1024
    .name:           _Z17select_bin_kernelPKjPi
    .private_segment_fixed_size: 0
    .sgpr_count:     23
    .sgpr_spill_count: 0
    .symbol:         _Z17select_bin_kernelPKjPi.kd
    .uniform_work_group_size: 1
    .uses_dynamic_stack: false
    .vgpr_count:     13
    .vgpr_spill_count: 0
    .wavefront_size: 64
  - .agpr_count:     0
    .args:
      - .actual_access:  read_only
        .address_space:  global
        .offset:         0
        .size:           8
        .value_kind:     global_buffer
      - .actual_access:  read_only
        .address_space:  global
        .offset:         8
        .size:           8
        .value_kind:     global_buffer
      - .address_space:  global
        .offset:         16
        .size:           8
        .value_kind:     global_buffer
      - .actual_access:  write_only
        .address_space:  global
        .offset:         24
        .size:           8
        .value_kind:     global_buffer
    .group_segment_fixed_size: 2052
    .kernarg_segment_align: 8
    .kernarg_segment_size: 32
    .language:       OpenCL C
    .language_version:
      - 2
      - 0
    .max_flat_workgroup_size: 512
    .name:           _Z14collect_kernelPKjS0_PiS1_
    .private_segment_fixed_size: 0
    .sgpr_count:     70
    .sgpr_spill_count: 0
    .symbol:         _Z14collect_kernelPKjS0_PiS1_.kd
    .uniform_work_group_size: 1
    .uses_dynamic_stack: false
    .vgpr_count:     34
    .vgpr_spill_count: 0
    .wavefront_size: 64
  - .agpr_count:     0
    .args:
      - .actual_access:  read_only
        .address_space:  global
        .offset:         0
        .size:           8
        .value_kind:     global_buffer
      - .actual_access:  read_only
        .address_space:  global
        .offset:         8
        .size:           8
        .value_kind:     global_buffer
      - .actual_access:  read_only
        .address_space:  global
        .offset:         16
        .size:           8
        .value_kind:     global_buffer
      - .actual_access:  read_only
        .address_space:  global
        .offset:         24
        .size:           8
        .value_kind:     global_buffer
      - .actual_access:  write_only
        .address_space:  global
        .offset:         32
        .size:           8
        .value_kind:     global_buffer
    .group_segment_fixed_size: 49664
    .kernarg_segment_align: 8
    .kernarg_segment_size: 40
    .language:       OpenCL C
    .language_version:
      - 2
      - 0
    .max_flat_workgroup_size: 1024
    .name:           _Z11rank_kernelPKfS0_PKiS2_Pi
    .private_segment_fixed_size: 0
    .sgpr_count:     23
    .sgpr_spill_count: 0
    .symbol:         _Z11rank_kernelPKfS0_PKiS2_Pi.kd
    .uniform_work_group_size: 1
    .uses_dynamic_stack: false
    .vgpr_count:     12
    .vgpr_spill_count: 0
    .wavefront_size: 64
  - .agpr_count:     0
    .args:
      - .actual_access:  read_only
        .address_space:  global
        .offset:         0
        .size:           8
        .value_kind:     global_buffer
      - .actual_access:  read_only
        .address_space:  global
        .offset:         8
        .size:           8
        .value_kind:     global_buffer
      - .actual_access:  write_only
        .address_space:  global
        .offset:         16
        .size:           8
        .value_kind:     global_buffer
      - .actual_access:  write_only
        .address_space:  global
        .offset:         24
        .size:           8
        .value_kind:     global_buffer
    .group_segment_fixed_size: 0
    .kernarg_segment_align: 8
    .kernarg_segment_size: 32
    .language:       OpenCL C
    .language_version:
      - 2
      - 0
    .max_flat_workgroup_size: 256
    .name:           _Z15prep_kvw_kernelPKfS0_PDF16_S1_
    .private_segment_fixed_size: 0
    .sgpr_count:     14
    .sgpr_spill_count: 0
    .symbol:         _Z15prep_kvw_kernelPKfS0_PDF16_S1_.kd
    .uniform_work_group_size: 1
    .uses_dynamic_stack: false
    .vgpr_count:     7
    .vgpr_spill_count: 0
    .wavefront_size: 64
  - .agpr_count:     0
    .args:
      - .actual_access:  read_only
        .address_space:  global
        .offset:         0
        .size:           8
        .value_kind:     global_buffer
      - .actual_access:  read_only
        .address_space:  global
        .offset:         8
        .size:           8
        .value_kind:     global_buffer
      - .actual_access:  read_only
        .address_space:  global
        .offset:         16
        .size:           8
        .value_kind:     global_buffer
      - .actual_access:  read_only
        .address_space:  global
        .offset:         24
        .size:           8
        .value_kind:     global_buffer
      - .actual_access:  write_only
        .address_space:  global
        .offset:         32
        .size:           8
        .value_kind:     global_buffer
    .group_segment_fixed_size: 67856
    .kernarg_segment_align: 8
    .kernarg_segment_size: 40
    .language:       OpenCL C
    .language_version:
      - 2
      - 0
    .max_flat_workgroup_size: 448
    .name:           _Z17cross_attn_kernelPKDF16_S0_S0_S0_Pf
    .private_segment_fixed_size: 0
    .sgpr_count:     26
    .sgpr_spill_count: 0
    .symbol:         _Z17cross_attn_kernelPKDF16_S0_S0_S0_Pf.kd
    .uniform_work_group_size: 1
    .uses_dynamic_stack: false
    .vgpr_count:     74
    .vgpr_spill_count: 0
    .wavefront_size: 64
  - .agpr_count:     0
    .args:
      - .offset:         0
        .size:           424
        .value_kind:     by_value
      - .offset:         424
        .size:           88
        .value_kind:     by_value
    .group_segment_fixed_size: 137216
    .kernarg_segment_align: 8
    .kernarg_segment_size: 512
    .language:       OpenCL C
    .language_version:
      - 2
      - 0
    .max_flat_workgroup_size: 512
    .name:           _Z12tailA_kernel5TailP3KvP
    .private_segment_fixed_size: 0
    .sgpr_count:     44
    .sgpr_spill_count: 0
    .symbol:         _Z12tailA_kernel5TailP3KvP.kd
    .uniform_work_group_size: 1
    .uses_dynamic_stack: false
    .vgpr_count:     200
    .vgpr_spill_count: 0
    .wavefront_size: 64
  - .agpr_count:     0
    .args:
      - .offset:         0
        .size:           424
        .value_kind:     by_value
      - .offset:         424
        .size:           88
        .value_kind:     by_value
    .group_segment_fixed_size: 146592
    .kernarg_segment_align: 8
    .kernarg_segment_size: 512
    .language:       OpenCL C
    .language_version:
      - 2
      - 0
    .max_flat_workgroup_size: 512
    .name:           _Z12tailB_kernel5TailP3KvP
    .private_segment_fixed_size: 0
    .sgpr_count:     44
    .sgpr_spill_count: 0
    .symbol:         _Z12tailB_kernel5TailP3KvP.kd
    .uniform_work_group_size: 1
    .uses_dynamic_stack: false
    .vgpr_count:     216
    .vgpr_spill_count: 0
    .wavefront_size: 64
  - .agpr_count:     0
    .args:
      - .offset:         0
        .size:           424
        .value_kind:     by_value
    .group_segment_fixed_size: 36896
    .kernarg_segment_align: 8
    .kernarg_segment_size: 424
    .language:       OpenCL C
    .language_version:
      - 2
      - 0
    .max_flat_workgroup_size: 512
    .name:           _Z12tailC_kernel5TailP
    .private_segment_fixed_size: 0
    .sgpr_count:     58
    .sgpr_spill_count: 0
    .symbol:         _Z12tailC_kernel5TailP.kd
    .uniform_work_group_size: 1
    .uses_dynamic_stack: false
    .vgpr_count:     115
    .vgpr_spill_count: 0
    .wavefront_size: 64
  - .agpr_count:     0
    .args:
      - .offset:         0
        .size:           344
        .value_kind:     by_value
    .group_segment_fixed_size: 0
    .kernarg_segment_align: 8
    .kernarg_segment_size: 344
    .language:       OpenCL C
    .language_version:
      - 2
      - 0
    .max_flat_workgroup_size: 256
    .name:           _Z15prep_all_kernel5PrepP
    .private_segment_fixed_size: 0
    .sgpr_count:     31
    .sgpr_spill_count: 0
    .symbol:         _Z15prep_all_kernel5PrepP.kd
    .uniform_work_group_size: 1
    .uses_dynamic_stack: false
    .vgpr_count:     39
    .vgpr_spill_count: 0
    .wavefront_size: 64
  - .agpr_count:     0
    .args:
      - .actual_access:  read_only
        .address_space:  global
        .offset:         0
        .size:           8
        .value_kind:     global_buffer
      - .actual_access:  read_only
        .address_space:  global
        .offset:         8
        .size:           8
        .value_kind:     global_buffer
      - .actual_access:  read_only
        .address_space:  global
        .offset:         16
        .size:           8
        .value_kind:     global_buffer
      - .actual_access:  read_only
        .address_space:  global
        .offset:         24
        .size:           8
        .value_kind:     global_buffer
      - .actual_access:  read_only
        .address_space:  global
        .offset:         32
        .size:           8
        .value_kind:     global_buffer
      - .actual_access:  write_only
        .address_space:  global
        .offset:         40
        .size:           8
        .value_kind:     global_buffer
      - .actual_access:  read_only
        .address_space:  global
        .offset:         48
        .size:           8
        .value_kind:     global_buffer
      - .actual_access:  read_only
        .address_space:  global
        .offset:         56
        .size:           8
        .value_kind:     global_buffer
    .group_segment_fixed_size: 130304
    .kernarg_segment_align: 8
    .kernarg_segment_size: 64
    .language:       OpenCL C
    .language_version:
      - 2
      - 0
    .max_flat_workgroup_size: 512
    .name:           _Z11conv_kernelILi8ELi128ELi0EEvPK15HIP_vector_typeIjLj4EES3_PKfS5_S5_PDF16_PfS7_
    .private_segment_fixed_size: 0
    .sgpr_count:     30
    .sgpr_spill_count: 0
    .symbol:         _Z11conv_kernelILi8ELi128ELi0EEvPK15HIP_vector_typeIjLj4EES3_PKfS5_S5_PDF16_PfS7_.kd
    .uniform_work_group_size: 1
    .uses_dynamic_stack: false
    .vgpr_count:     254
    .vgpr_spill_count: 0
    .wavefront_size: 64
